# on top of cq hoist: Wv fragment loads spread through the exp/sum and y phases (scores phase now LDS-conflict-free)
# baseline (speedup 1.0000x reference)
_Z7na_mainPKDF16_PKhS0_PKfS4_S4_S4_Pf:
	s_lshl_b32 s3, s2, 5
	s_and_b32 s3, s3, 0xe0
	s_ashr_i32 s2, s2, 3
	s_add_i32 s3, s3, s2
	s_ashr_i32 s2, s3, 6
	s_lshl_b32 s3, s3, 5
	s_and_b32 s14, s3, 0x7e0
	v_mov_b32_e32 v1, 0x7c0
	s_load_dwordx8 s[4:11], s[0:1], 0x0
	s_load_dwordx2 s[18:19], s[0:1], 0x20
	v_med3_u32 v1, s14, 32, v1
	v_subrev_u32_e32 v97, 32, v1
	s_ashr_i32 s3, s2, 31
	v_lshlrev_b32_e32 v58, 1, v97
	s_lshl_b64 s[12:13], s[2:3], 12
	v_mov_b32_e32 v59, 0
	v_sub_u32_e32 v60, s14, v97
	v_lshl_add_u64 v[10:11], s[12:13], 0, v[58:59]
	v_lshlrev_b64 v[2:3], 9, v[10:11]
	v_lshl_or_b32 v22, v60, 6, v0
	s_waitcnt lgkmcnt(0)
	s_mov_b32 s20, s8
	s_mov_b32 s21, s9
	v_and_b32_e32 v208, 31, v0
	v_lshlrev_b32_e32 v208, 5, v208
	global_load_dwordx4 v[192:195], v208, s[18:19]
	global_load_dwordx4 v[196:199], v208, s[18:19] offset:16
	v_lshl_add_u64 v[20:21], s[4:5], 0, v[2:3]
	v_ashrrev_i32_e32 v23, 31, v22
	v_lshl_add_u64 v[2:3], v[22:23], 4, v[20:21]
	global_load_dwordx4 v[12:15], v[2:3], off
	v_or_b32_e32 v28, 0x200, v22
	v_ashrrev_i32_e32 v29, 31, v28
	v_lshl_add_u64 v[2:3], v[28:29], 4, v[20:21]
	global_load_dwordx4 v[16:19], v[2:3], off
	v_or_b32_e32 v184, 0x400, v22
	v_ashrrev_i32_e32 v185, 31, v184
	v_lshl_add_u64 v[184:185], v[184:185], 4, v[20:21]
	v_or_b32_e32 v188, 0x600, v22
	v_ashrrev_i32_e32 v189, 31, v188
	v_lshl_add_u64 v[188:189], v[188:189], 4, v[20:21]
	global_load_dwordx4 v[184:187], v[184:185], off
	global_load_dwordx4 v[188:191], v[188:189], off
	v_lshrrev_b32_e32 v99, 6, v0
	v_and_b32_e32 v98, 63, v0
	v_lshlrev_b32_e32 v118, 13, v99
	v_lshl_or_b32 v58, v98, 5, v118
	s_movk_i32 s15, 0x1000
	v_lshl_add_u64 v[24:25], s[6:7], 0, v[58:59]
	v_or_b32_e32 v32, 0x400, v22
	v_or_b32_e32 v62, 0x600, v22
	v_add_co_u32_e32 v64, vcc, s15, v24
	s_mov_b64 s[12:13], 0x1000
	s_mov_b64 s[16:17], 0x1800
	v_lshlrev_b32_e32 v72, 1, v60
	v_lshrrev_b32_e32 v23, 5, v22
	v_and_b32_e32 v34, 32, v22
	v_ashrrev_i32_e32 v33, 31, v32
	v_ashrrev_i32_e32 v63, 31, v62
	v_addc_co_u32_e32 v65, vcc, 0, v25, vcc
	global_load_dwordx4 v[6:9], v58, s[6:7] offset:16
	global_load_dwordx4 v[2:5], v58, s[6:7]
	global_load_dwordx4 v[54:57], v58, s[6:7] offset:2064
	global_load_dwordx4 v[50:53], v58, s[6:7] offset:2048
	v_lshrrev_b32_e32 v58, 6, v22
	v_bfe_u32 v73, v22, 8, 2
	v_lshl_add_u64 v[26:27], v[24:25], 0, s[12:13]
	v_lshl_add_u64 v[24:25], v[24:25], 0, s[16:17]
	v_cmp_ne_u32_e32 vcc, 0, v34
	v_sub_u32_e32 v75, v23, v72
	global_load_dwordx4 v[42:45], v[64:65], off
	global_load_dwordx4 v[46:49], v[26:27], off offset:16
	global_load_dwordx4 v[34:37], v[64:65], off offset:2048
	global_load_dwordx4 v[38:41], v[24:25], off offset:16
	v_mov_b32_e32 v61, 0x60
	v_cndmask_b32_e32 v74, 0, v61, vcc
	v_add_u32_e32 v33, v74, v58
	v_lshlrev_b32_e32 v64, 2, v33
	v_bfe_u32 v96, v0, 4, 1
	v_and_b32_e32 v100, 15, v0
	v_mov_b32_e32 v30, v59
	v_mov_b32_e32 v31, v59
	v_and_b32_e32 v64, 12, v64
	v_mul_u32_u24_e32 v29, 0xc000, v96
	v_bitop3_b32 v64, v64, v100, v73 bitop3:0x36
	v_lshl_or_b32 v64, v64, 4, v29
	v_lshlrev_b32_e32 v63, 1, v75
	v_lshl_add_u32 v33, v33, 8, v64
	v_bfe_u32 v71, v0, 1, 4
	v_and_b32_e32 v70, 32, v0
	v_lshlrev_b32_e32 v1, 3, v0
	v_lshrrev_b32_e32 v58, 1, v75
	v_and_b32_e32 v1, 8, v1
	v_add_lshl_u32 v58, v58, v70, 8
	v_lshlrev_b32_e32 v121, 3, v99
	v_bfe_u32 v101, v0, 4, 2
	v_lshlrev_b32_e32 v102, 2, v101
	v_and_b32_e32 v116, 31, v0
	v_bfe_u32 v119, v0, 5, 1
	v_lshlrev_b32_e32 v124, 1, v119
	v_lshlrev_b32_e32 v117, 8, v116
	v_lshrrev_b32_e32 v95, 4, v0
	s_movk_i32 s16, 0x60
	s_mov_b32 s17, 0xc000
	v_and_b32_e32 v211, 3, v99
	v_lshrrev_b32_e32 v212, 2, v99
	v_lshl_or_b32 v211, v211, 2, v212
	v_xor_b32_e32 v213, v100, v211
	v_mul_u32_u24_e32 v214, 0x60, v119
	v_add3_u32 v214, v214, v60, v99
	v_mul_u32_u24_e32 v215, 0xc000, v96
	v_lshl_add_u32 v214, v214, 8, v215
	v_lshl_or_b32 v220, v213, 4, v214
	v_xor_b32_e32 v221, 32, v220
	v_xor_b32_e32 v216, v71, v211
	v_lshl_add_u32 v217, v119, 5, v99
	v_lshlrev_b32_e32 v217, 8, v217
	v_lshl_or_b32 v216, v216, 4, v217
	v_or_b32_e32 v216, v216, v1
	v_add_u32_e32 v222, 0x23800, v216
	v_xor_b32_e32 v223, 32, v222
	s_waitcnt vmcnt(11)
	ds_write_b128 v220, v[12:15]
	v_fma_mix_f32 v200, v192, v12, 0 op_sel_hi:[0,1,0]
	v_fma_mix_f32 v201, v193, v12, 0 op_sel:[0,1,0] op_sel_hi:[0,1,0]
	v_cvt_f32_f16_e32 v211, v12
	v_cvt_f32_f16_sdwa v212, v12 dst_sel:DWORD dst_unused:UNUSED_PAD src0_sel:WORD_1
	v_fma_mix_f32 v200, v194, v13, v200 op_sel_hi:[0,1,0]
	v_fma_mix_f32 v201, v195, v13, v201 op_sel:[0,1,0] op_sel_hi:[0,1,0]
	v_cvt_f32_f16_e32 v213, v13
	v_cvt_f32_f16_sdwa v214, v13 dst_sel:DWORD dst_unused:UNUSED_PAD src0_sel:WORD_1
	v_fma_mix_f32 v200, v196, v14, v200 op_sel_hi:[0,1,0]
	v_fma_mix_f32 v201, v197, v14, v201 op_sel:[0,1,0] op_sel_hi:[0,1,0]
	v_cvt_f32_f16_e32 v215, v14
	v_cvt_f32_f16_sdwa v216, v14 dst_sel:DWORD dst_unused:UNUSED_PAD src0_sel:WORD_1
	v_fma_mix_f32 v200, v198, v15, v200 op_sel_hi:[0,1,0]
	v_fma_mix_f32 v201, v199, v15, v201 op_sel:[0,1,0] op_sel_hi:[0,1,0]
	v_cvt_f32_f16_e32 v217, v15
	v_cvt_f32_f16_sdwa v218, v15 dst_sel:DWORD dst_unused:UNUSED_PAD src0_sel:WORD_1
	v_cvt_pk_fp8_f32 v224, v211, v212
	v_cvt_pk_fp8_f32 v225, v215, v216
	v_cvt_pk_fp8_f32 v224, v213, v214 op_sel:[0,0,1]
	v_cvt_pk_fp8_f32 v225, v217, v218 op_sel:[0,0,1]
	s_nop 0
	ds_write_b64 v222, v[224:225]
	s_waitcnt vmcnt(10)
	ds_write_b128 v221, v[16:19] offset:2048
	v_fma_mix_f32 v202, v192, v16, 0 op_sel_hi:[0,1,0]
	v_fma_mix_f32 v203, v193, v16, 0 op_sel:[0,1,0] op_sel_hi:[0,1,0]
	v_cvt_f32_f16_e32 v211, v16
	v_cvt_f32_f16_sdwa v212, v16 dst_sel:DWORD dst_unused:UNUSED_PAD src0_sel:WORD_1
	v_fma_mix_f32 v202, v194, v17, v202 op_sel_hi:[0,1,0]
	v_fma_mix_f32 v203, v195, v17, v203 op_sel:[0,1,0] op_sel_hi:[0,1,0]
	v_cvt_f32_f16_e32 v213, v17
	v_cvt_f32_f16_sdwa v214, v17 dst_sel:DWORD dst_unused:UNUSED_PAD src0_sel:WORD_1
	v_fma_mix_f32 v202, v196, v18, v202 op_sel_hi:[0,1,0]
	v_fma_mix_f32 v203, v197, v18, v203 op_sel:[0,1,0] op_sel_hi:[0,1,0]
	v_cvt_f32_f16_e32 v215, v18
	v_cvt_f32_f16_sdwa v216, v18 dst_sel:DWORD dst_unused:UNUSED_PAD src0_sel:WORD_1
	v_fma_mix_f32 v202, v198, v19, v202 op_sel_hi:[0,1,0]
	v_fma_mix_f32 v203, v199, v19, v203 op_sel:[0,1,0] op_sel_hi:[0,1,0]
	v_cvt_f32_f16_e32 v217, v19
	v_cvt_f32_f16_sdwa v218, v19 dst_sel:DWORD dst_unused:UNUSED_PAD src0_sel:WORD_1
	v_cvt_pk_fp8_f32 v226, v211, v212
	v_cvt_pk_fp8_f32 v227, v215, v216
	v_cvt_pk_fp8_f32 v226, v213, v214 op_sel:[0,0,1]
	v_cvt_pk_fp8_f32 v227, v217, v218 op_sel:[0,0,1]
	s_nop 0
	ds_write_b64 v223, v[226:227] offset:2048
	s_waitcnt vmcnt(9)
	ds_write_b128 v220, v[184:187] offset:4096
	v_fma_mix_f32 v204, v192, v184, 0 op_sel_hi:[0,1,0]
	v_fma_mix_f32 v205, v193, v184, 0 op_sel:[0,1,0] op_sel_hi:[0,1,0]
	v_cvt_f32_f16_e32 v211, v184
	v_cvt_f32_f16_sdwa v212, v184 dst_sel:DWORD dst_unused:UNUSED_PAD src0_sel:WORD_1
	v_fma_mix_f32 v204, v194, v185, v204 op_sel_hi:[0,1,0]
	v_fma_mix_f32 v205, v195, v185, v205 op_sel:[0,1,0] op_sel_hi:[0,1,0]
	v_cvt_f32_f16_e32 v213, v185
	v_cvt_f32_f16_sdwa v214, v185 dst_sel:DWORD dst_unused:UNUSED_PAD src0_sel:WORD_1
	v_fma_mix_f32 v204, v196, v186, v204 op_sel_hi:[0,1,0]
	v_fma_mix_f32 v205, v197, v186, v205 op_sel:[0,1,0] op_sel_hi:[0,1,0]
	v_cvt_f32_f16_e32 v215, v186
	v_cvt_f32_f16_sdwa v216, v186 dst_sel:DWORD dst_unused:UNUSED_PAD src0_sel:WORD_1
	v_fma_mix_f32 v204, v198, v187, v204 op_sel_hi:[0,1,0]
	v_fma_mix_f32 v205, v199, v187, v205 op_sel:[0,1,0] op_sel_hi:[0,1,0]
	v_cvt_f32_f16_e32 v217, v187
	v_cvt_f32_f16_sdwa v218, v187 dst_sel:DWORD dst_unused:UNUSED_PAD src0_sel:WORD_1
	v_cvt_pk_fp8_f32 v228, v211, v212
	v_cvt_pk_fp8_f32 v229, v215, v216
	v_cvt_pk_fp8_f32 v228, v213, v214 op_sel:[0,0,1]
	v_cvt_pk_fp8_f32 v229, v217, v218 op_sel:[0,0,1]
	s_nop 0
	ds_write_b64 v222, v[228:229] offset:4096
	s_waitcnt vmcnt(8)
	ds_write_b128 v221, v[188:191] offset:6144
	v_fma_mix_f32 v206, v192, v188, 0 op_sel_hi:[0,1,0]
	v_fma_mix_f32 v207, v193, v188, 0 op_sel:[0,1,0] op_sel_hi:[0,1,0]
	v_cvt_f32_f16_e32 v211, v188
	v_cvt_f32_f16_sdwa v212, v188 dst_sel:DWORD dst_unused:UNUSED_PAD src0_sel:WORD_1
	v_fma_mix_f32 v206, v194, v189, v206 op_sel_hi:[0,1,0]
	v_fma_mix_f32 v207, v195, v189, v207 op_sel:[0,1,0] op_sel_hi:[0,1,0]
	v_cvt_f32_f16_e32 v213, v189
	v_cvt_f32_f16_sdwa v214, v189 dst_sel:DWORD dst_unused:UNUSED_PAD src0_sel:WORD_1
	v_fma_mix_f32 v206, v196, v190, v206 op_sel_hi:[0,1,0]
	v_fma_mix_f32 v207, v197, v190, v207 op_sel:[0,1,0] op_sel_hi:[0,1,0]
	v_cvt_f32_f16_e32 v215, v190
	v_cvt_f32_f16_sdwa v216, v190 dst_sel:DWORD dst_unused:UNUSED_PAD src0_sel:WORD_1
	v_fma_mix_f32 v206, v198, v191, v206 op_sel_hi:[0,1,0]
	v_fma_mix_f32 v207, v199, v191, v207 op_sel:[0,1,0] op_sel_hi:[0,1,0]
	v_cvt_f32_f16_e32 v217, v191
	v_cvt_f32_f16_sdwa v218, v191 dst_sel:DWORD dst_unused:UNUSED_PAD src0_sel:WORD_1
	v_cvt_pk_fp8_f32 v230, v211, v212
	v_cvt_pk_fp8_f32 v231, v215, v216
	v_cvt_pk_fp8_f32 v230, v213, v214 op_sel:[0,0,1]
	v_cvt_pk_fp8_f32 v231, v217, v218 op_sel:[0,0,1]
	s_nop 0
	ds_write_b64 v223, v[230:231] offset:6144
	v_add_f32_e32 v200, v200, v201
	v_add_f32_e32 v202, v202, v203
	v_add_f32_e32 v204, v204, v205
	v_add_f32_e32 v206, v206, v207
	v_lshlrev_b32_e32 v208, 7, v119
	v_lshl_add_u32 v208, v99, 2, v208
	v_add_u32_e32 v208, 0x27800, v208
	v_add_f32_dpp v200, v200, v200 quad_perm:[1,0,3,2] row_mask:0xf bank_mask:0xf
	v_add_f32_dpp v202, v202, v202 quad_perm:[1,0,3,2] row_mask:0xf bank_mask:0xf
	v_add_f32_dpp v204, v204, v204 quad_perm:[1,0,3,2] row_mask:0xf bank_mask:0xf
	v_add_f32_dpp v206, v206, v206 quad_perm:[1,0,3,2] row_mask:0xf bank_mask:0xf
	v_add_f32_dpp v200, v200, v200 quad_perm:[2,3,0,1] row_mask:0xf bank_mask:0xf
	v_add_f32_dpp v202, v202, v202 quad_perm:[2,3,0,1] row_mask:0xf bank_mask:0xf
	v_add_f32_dpp v204, v204, v204 quad_perm:[2,3,0,1] row_mask:0xf bank_mask:0xf
	v_add_f32_dpp v206, v206, v206 quad_perm:[2,3,0,1] row_mask:0xf bank_mask:0xf
	v_add_f32_dpp v200, v200, v200 row_half_mirror row_mask:0xf bank_mask:0xf
	v_add_f32_dpp v202, v202, v202 row_half_mirror row_mask:0xf bank_mask:0xf
	v_add_f32_dpp v204, v204, v204 row_half_mirror row_mask:0xf bank_mask:0xf
	v_add_f32_dpp v206, v206, v206 row_half_mirror row_mask:0xf bank_mask:0xf
	v_add_f32_dpp v200, v200, v200 row_mirror row_mask:0xf bank_mask:0xf
	v_add_f32_dpp v202, v202, v202 row_mirror row_mask:0xf bank_mask:0xf
	v_add_f32_dpp v204, v204, v204 row_mirror row_mask:0xf bank_mask:0xf
	v_add_f32_dpp v206, v206, v206 row_mirror row_mask:0xf bank_mask:0xf
	v_add_f32_dpp v200, v200, v200 row_bcast:15 row_mask:0xa bank_mask:0xf
	v_add_f32_dpp v202, v202, v202 row_bcast:15 row_mask:0xa bank_mask:0xf
	v_add_f32_dpp v204, v204, v204 row_bcast:15 row_mask:0xa bank_mask:0xf
	v_add_f32_dpp v206, v206, v206 row_bcast:15 row_mask:0xa bank_mask:0xf
	s_mov_b32 exec_lo, 0xffff0000
	s_mov_b32 exec_hi, 0xffff0000
	ds_write_b32 v208, v200
	ds_write_b32 v208, v202 offset:32
	ds_write_b32 v208, v204 offset:64
	ds_write_b32 v208, v206 offset:96
	s_mov_b64 exec, -1
	v_lshlrev_b32_e32 v201, 7, v99
	v_lshl_or_b32 v201, v119, 4, v201
	global_load_dwordx4 v[184:187], v201, s[10:11]
	global_load_dwordx4 v[188:191], v201, s[10:11] offset:32
	global_load_dwordx4 v[192:195], v201, s[10:11] offset:64
	global_load_dwordx4 v[196:199], v201, s[10:11] offset:96
	v_cmp_lt_i32_e32 vcc, v121, v60
	s_nop 0
	v_mov_b32_e32 v15, v59
	v_cndmask_b32_e64 v12, 32, 0, vcc
	v_add_u32_e32 v16, v12, v121
	v_or_b32_e32 v12, v16, v101
	v_lshlrev_b32_e32 v58, 1, v12
	v_lshrrev_b32_e32 v12, 5, v0
	v_and_b32_e32 v12, 2, v12
	v_bitop3_b32 v14, v102, v100, v12 bitop3:0x36
	v_lshl_add_u64 v[12:13], v[10:11], 0, v[58:59]
	v_lshlrev_b64 v[12:13], 9, v[12:13]
	v_lshlrev_b32_e32 v16, 8, v16
	v_lshl_add_u64 v[12:13], s[4:5], 0, v[12:13]
	v_lshlrev_b32_e32 v14, 4, v14
	v_readfirstlane_b32 s6, v16
	v_add_u32_e32 v17, 0xc000, v16
	v_lshl_add_u64 v[12:13], v[12:13], 0, v[14:15]
	s_mov_b32 m0, s6
	s_mov_b64 s[6:7], 0x100
	v_readfirstlane_b32 s12, v17
	global_load_lds_dwordx4 v[12:13], off
	v_lshl_add_u64 v[12:13], v[12:13], 0, s[6:7]
	s_mov_b32 m0, s12
	v_or_b32_e32 v58, 1, v58
	global_load_lds_dwordx4 v[12:13], off
	v_lshl_add_u64 v[12:13], v[10:11], 0, v[58:59]
	v_lshlrev_b64 v[12:13], 9, v[12:13]
	v_lshl_add_u64 v[12:13], s[4:5], 0, v[12:13]
	v_lshl_add_u64 v[12:13], v[12:13], 0, v[14:15]
	v_add_u32_e32 v14, 0x6000, v16
	v_bfe_u32 v61, v0, 2, 2
	v_readfirstlane_b32 s12, v14
	v_add_u32_e32 v14, 0x12000, v16
	s_mov_b32 m0, s12
	v_readfirstlane_b32 s12, v14
	global_load_lds_dwordx4 v[12:13], off
	v_lshl_add_u64 v[12:13], v[12:13], 0, s[6:7]
	s_mov_b32 m0, s12
	v_add_u32_e32 v18, 0x23800, v117
	global_load_lds_dwordx4 v[12:13], off
	v_or_b32_e32 v12, 4, v121
	v_cmp_lt_i32_e32 vcc, v12, v60
	s_nop 1
	v_cndmask_b32_e64 v13, 32, 0, vcc
	v_add_u32_e32 v16, v13, v12
	v_or_b32_e32 v13, v16, v101
	v_lshlrev_b32_e32 v58, 1, v13
	v_bfe_u32 v12, v12, 2, 2
	v_bitop3_b32 v14, v102, v100, v12 bitop3:0x36
	v_lshl_add_u64 v[12:13], v[10:11], 0, v[58:59]
	v_lshlrev_b64 v[12:13], 9, v[12:13]
	v_lshlrev_b32_e32 v16, 8, v16
	v_lshl_add_u64 v[12:13], s[4:5], 0, v[12:13]
	v_lshlrev_b32_e32 v14, 4, v14
	v_readfirstlane_b32 s12, v16
	v_add_u32_e32 v17, 0xc000, v16
	v_lshl_add_u64 v[12:13], v[12:13], 0, v[14:15]
	s_mov_b32 m0, s12
	v_readfirstlane_b32 s12, v17
	v_or_b32_e32 v58, 1, v58
	global_load_lds_dwordx4 v[12:13], off
	v_lshl_add_u64 v[12:13], v[12:13], 0, s[6:7]
	s_mov_b32 m0, s12
	v_lshl_add_u64 v[10:11], v[10:11], 0, v[58:59]
	global_load_lds_dwordx4 v[12:13], off
	v_lshlrev_b64 v[10:11], 9, v[10:11]
	v_add_u32_e32 v12, 0x6000, v16
	v_lshl_add_u64 v[10:11], s[4:5], 0, v[10:11]
	v_readfirstlane_b32 s4, v12
	v_add_u32_e32 v12, 0x12000, v16
	v_lshl_add_u64 v[10:11], v[10:11], 0, v[14:15]
	s_mov_b32 m0, s4
	v_readfirstlane_b32 s4, v12
	global_load_lds_dwordx4 v[10:11], off
	v_lshl_add_u64 v[10:11], v[10:11], 0, s[6:7]
	s_mov_b32 m0, s4
	s_nop 0
	global_load_lds_dwordx4 v[10:11], off
	s_waitcnt lgkmcnt(0)
	s_barrier
	v_lshlrev_b32_e32 v10, 2, v0
	v_and_b32_e32 v94, 12, v10
	v_or_b32_e32 v120, v94, v61
	v_bitop3_b32 v10, v124, v94, v61 bitop3:0x1e
	v_lshl_or_b32 v14, v10, 4, v18
	v_bitop3_b32 v10, v124, v120, 1 bitop3:0x36
	v_lshl_or_b32 v19, v10, 4, v18
	s_load_dwordx4 s[4:7], s[0:1], 0x20
	s_load_dwordx2 s[12:13], s[0:1], 0x38
	ds_read_b128 v[10:13], v14
	ds_read_b128 v[62:65], v14 offset:8192
	ds_read_b128 v[14:17], v19
	ds_read_b128 v[66:69], v19 offset:8192
	v_bitop3_b32 v19, v124, v120, 4 bitop3:0x36
	v_lshl_or_b32 v19, v19, 4, v18
	v_bitop3_b32 v20, v124, v120, 5 bitop3:0x36
	v_lshl_or_b32 v20, v20, 4, v18
	ds_read_b128 v[70:73], v19
	ds_read_b128 v[78:81], v19 offset:8192
	ds_read_b128 v[74:77], v20
	ds_read_b128 v[82:85], v20 offset:8192
	v_bitop3_b32 v19, v124, v120, 8 bitop3:0x36
	v_lshl_or_b32 v19, v19, 4, v18
	v_bitop3_b32 v20, v124, v120, 9 bitop3:0x36
	v_lshl_or_b32 v20, v20, 4, v18
	ds_read_b128 v[86:89], v19
	ds_read_b128 v[104:107], v19 offset:8192
	ds_read_b128 v[90:93], v20
	ds_read_b128 v[108:111], v20 offset:8192
	v_bitop3_b32 v19, v124, v120, 12 bitop3:0x36
	v_lshl_or_b32 v19, v19, 4, v18
	v_bitop3_b32 v20, v124, v120, 13 bitop3:0x36
	v_lshl_or_b32 v18, v20, 4, v18
	ds_read_b128 v[126:129], v19
	ds_read_b128 v[134:137], v19 offset:8192
	ds_read_b128 v[130:133], v18
	ds_read_b128 v[138:141], v18 offset:8192
	v_mov_b32_e32 v103, 0x7f
	v_lshlrev_b32_e32 v58, 7, v99
	v_or_b32_e32 v122, 0x18000, v117
	s_waitcnt vmcnt(12) lgkmcnt(0)
	v_mfma_scale_f32_32x32x64_f8f6f4 v[18:33], v[2:9], v[10:17], 0, v103, v103 op_sel_hi:[0,0,0]
	v_lshlrev_b32_e32 v125, 3, v119
	v_or_b32_e32 v123, 0x1a000, v117
	v_mfma_scale_f32_32x32x64_f8f6f4 v[2:17], v[2:9], v[62:69], 0, v103, v103 op_sel_hi:[0,0,0]
	v_and_b32_e32 v62, 12, v95
	v_mfma_scale_f32_32x32x64_f8f6f4 v[18:33], v[50:57], v[70:77], v[18:33], v103, v103 op_sel_hi:[0,0,0]
	v_mfma_scale_f32_32x32x64_f8f6f4 v[2:17], v[50:57], v[78:85], v[2:17], v103, v103 op_sel_hi:[0,0,0]
	s_brev_b32 s10, 60
	v_lshlrev_b32_e32 v58, 6, v0
	v_and_b32_e32 v58, 0x4000, v58
	v_or3_b32 v63, v122, v58, v125
	v_or3_b32 v58, v123, v58, v125
	v_mfma_scale_f32_32x32x64_f8f6f4 v[18:33], v[42:49], v[86:93], v[18:33], v103, v103 op_sel_hi:[0,0,0]
	v_mfma_scale_f32_32x32x64_f8f6f4 v[2:17], v[42:49], v[104:111], v[2:17], v103, v103 op_sel_hi:[0,0,0]
	s_nop 0
	v_mfma_scale_f32_32x32x64_f8f6f4 v[2:17], v[34:41], v[134:141], v[2:17], v103, v103 op_sel_hi:[0,0,0]
	v_mfma_scale_f32_32x32x64_f8f6f4 v[18:33], v[34:41], v[126:133], v[18:33], v103, v103 op_sel_hi:[0,0,0]
	s_waitcnt vmcnt(8)
	s_nop 15
	s_nop 1
	v_fma_f32 v2, v2, s10, v184
	v_fma_f32 v3, v3, s10, v185
	v_fma_f32 v4, v4, s10, v186
	v_fma_f32 v5, v5, s10, v187
	v_cvt_pk_f16_f32 v2, v2, v3
	v_cvt_pk_f16_f32 v3, v4, v5
	v_bitop3_b32 v4, v95, v120, 12 bitop3:0x6c
	v_pk_fma_f32 v[18:19], v[18:19], s[10:11], v[184:185] op_sel_hi:[1,0,1]
	v_pk_fma_f32 v[20:21], v[20:21], s[10:11], v[186:187] op_sel_hi:[1,0,1]
	v_lshlrev_b32_e32 v4, 4, v4
	v_cvt_pk_f16_f32 v18, v18, v19
	v_cvt_pk_f16_f32 v19, v20, v21
	v_or_b32_e32 v5, v63, v4
	v_or_b32_e32 v4, v58, v4
	ds_write_b64 v5, v[18:19]
	ds_write_b64 v4, v[2:3]
	v_pk_fma_f32 v[2:3], v[22:23], s[10:11], v[188:189] op_sel_hi:[1,0,1]
	v_pk_fma_f32 v[4:5], v[6:7], s[10:11], v[188:189] op_sel_hi:[1,0,1]
	v_pk_fma_f32 v[6:7], v[24:25], s[10:11], v[190:191] op_sel_hi:[1,0,1]
	v_cvt_pk_f16_f32 v2, v2, v3
	v_cvt_pk_f16_f32 v3, v6, v7
	v_pk_fma_f32 v[6:7], v[8:9], s[10:11], v[190:191] op_sel_hi:[1,0,1]
	v_cvt_pk_f16_f32 v4, v4, v5
	v_cvt_pk_f16_f32 v5, v6, v7
	v_bitop3_b32 v6, v62, v120, 1 bitop3:0x36
	v_lshlrev_b32_e32 v6, 4, v6
	v_or_b32_e32 v7, v63, v6
	ds_write_b64 v7, v[2:3]
	v_or_b32_e32 v2, v58, v6
	ds_write_b64 v2, v[4:5]
	v_pk_fma_f32 v[2:3], v[26:27], s[10:11], v[192:193] op_sel_hi:[1,0,1]
	v_pk_fma_f32 v[6:7], v[28:29], s[10:11], v[194:195] op_sel_hi:[1,0,1]
	v_cvt_pk_f16_f32 v2, v2, v3
	v_pk_fma_f32 v[4:5], v[10:11], s[10:11], v[192:193] op_sel_hi:[1,0,1]
	v_cvt_pk_f16_f32 v3, v6, v7
	v_pk_fma_f32 v[6:7], v[12:13], s[10:11], v[194:195] op_sel_hi:[1,0,1]
	v_cvt_pk_f16_f32 v4, v4, v5
	v_cvt_pk_f16_f32 v5, v6, v7
	v_bitop3_b32 v6, v62, v120, 2 bitop3:0x36
	v_lshlrev_b32_e32 v6, 4, v6
	v_or_b32_e32 v7, v63, v6
	ds_write_b64 v7, v[2:3]
	v_or_b32_e32 v2, v58, v6
	ds_write_b64 v2, v[4:5]
	v_pk_fma_f32 v[2:3], v[30:31], s[10:11], v[196:197] op_sel_hi:[1,0,1]
	v_pk_fma_f32 v[6:7], v[32:33], s[10:11], v[198:199] op_sel_hi:[1,0,1]
	v_cvt_pk_f16_f32 v2, v2, v3
	v_pk_fma_f32 v[4:5], v[14:15], s[10:11], v[196:197] op_sel_hi:[1,0,1]
	v_cvt_pk_f16_f32 v3, v6, v7
	v_pk_fma_f32 v[6:7], v[16:17], s[10:11], v[198:199] op_sel_hi:[1,0,1]
	v_cvt_pk_f16_f32 v4, v4, v5
	v_cvt_pk_f16_f32 v5, v6, v7
	v_bitop3_b32 v6, v62, v120, 3 bitop3:0x36
	v_lshlrev_b32_e32 v6, 4, v6
	v_or_b32_e32 v7, v63, v6
	ds_write_b64 v7, v[2:3]
	v_or_b32_e32 v2, v58, v6
	ds_write_b64 v2, v[4:5]
	s_waitcnt vmcnt(0) lgkmcnt(0)
	s_barrier
	v_and_b32_e32 v236, 1, v101
	v_lshrrev_b32_e32 v237, 1, v101
	v_xor_b32_e32 v237, v237, v236
	v_lshl_or_b32 v236, v236, 1, v237
	v_lshrrev_b32_e32 v27, 8, v0
	v_lshrrev_b32_e32 v3, 3, v0
	v_and_b32_e32 v3, 16, v3
	v_mul_u32_u24_e32 v28, 0x60, v27
	v_lshlrev_b32_e32 v26, 5, v27
	v_or_b32_e32 v146, v3, v100
	v_or_b32_e32 v147, v28, v100
	v_or_b32_e32 v4, v146, v26
	v_lshlrev_b32_e32 v209, 2, v4
	v_add_u32_e32 v209, 0x27800, v209
	v_lshlrev_b32_e32 v4, 8, v4
	v_or_b32_e32 v5, 0x18000, v4
	v_bitop3_b32 v11, v236, v120, 12 bitop3:0x36
	v_or_b32_e32 v95, 0x1c000, v4
	v_lshlrev_b32_e32 v29, 3, v101
	v_bitop3_b32 v6, v236, v94, v61 bitop3:0x1e
	v_bitop3_b32 v8, v236, v120, 4 bitop3:0x36
	v_bitop3_b32 v10, v236, v120, 8 bitop3:0x36
	v_lshlrev_b32_e32 v94, 4, v11
	v_lshlrev_b32_e32 v6, 4, v6
	v_lshlrev_b32_e32 v8, 4, v8
	v_lshlrev_b32_e32 v58, 4, v10
	v_or_b32_e32 v7, v5, v6
	v_or_b32_e32 v9, v5, v8
	v_or_b32_e32 v10, v5, v58
	v_or_b32_e32 v5, v5, v94
	v_or_b32_e32 v6, v95, v6
	v_or_b32_e32 v60, v95, v8
	ds_read_b128 v[22:25], v7
	ds_read_b128 v[18:21], v9
	ds_read_b128 v[14:17], v10
	ds_read_b128 v[10:13], v5
	ds_read_b128 v[6:9], v6
	ds_read_b128 v[2:5], v60
	v_bfe_u32 v103, v0, 6, 1
	s_movk_i32 s5, 0x2000
	v_mad_u32_u24 v44, v103, 48, v147
	v_lshlrev_b32_e32 v60, 8, v44
	v_lshlrev_b32_e32 v44, 2, v44
	v_or_b32_e32 v35, v95, v58
	v_lshlrev_b32_e32 v58, 14, v99
	v_and_b32_e32 v44, 12, v44
	v_or_b32_e32 v56, v44, v61
	v_bitop3_b32 v44, v236, v44, v61 bitop3:0x1e
	v_lshl_add_u64 v[32:33], s[8:9], 0, v[58:59]
	v_lshlrev_b32_e32 v58, 4, v98
	v_or_b32_e32 v36, v95, v94
	v_lshl_add_u64 v[88:89], v[32:33], 0, v[58:59]
	v_lshl_or_b32 v57, v44, 4, v60
	ds_read_b128 v[40:43], v35
	ds_read_b128 v[106:109], v36
	s_load_dword s4, s[6:7], 0x0
	ds_read_b128 v[44:47], v57
	v_bitop3_b32 v48, v236, v56, 4 bitop3:0x36
	v_lshl_or_b32 v62, v48, 4, v60
	ds_read_b128 v[48:51], v62
	v_bitop3_b32 v52, v236, v56, 8 bitop3:0x36
	v_lshl_or_b32 v63, v52, 4, v60
	ds_read_b128 v[52:55], v63
	s_waitcnt lgkmcnt(0)
	v_mfma_f32_16x16x32_f16 v[44:47], v[44:47], v[22:25], 0
	v_bitop3_b32 v64, v236, v56, 12 bitop3:0x36
	ds_read_b128 v[56:59], v57 offset:49152
	v_lshl_or_b32 v60, v64, 4, v60
	v_mfma_f32_16x16x32_f16 v[44:47], v[48:51], v[18:21], v[44:47]
	ds_read_b128 v[68:71], v60
	ds_read_b128 v[72:75], v62 offset:49152
	v_mad_u32_u24 v104, v103, 3, 1
	v_lshlrev_b32_e32 v132, 4, v104
	v_mfma_f32_16x16x32_f16 v[44:47], v[52:55], v[14:17], v[44:47]
	v_add_u32_e32 v52, v132, v147
	ds_read_b128 v[76:79], v63 offset:49152
	ds_read_b128 v[80:83], v60 offset:49152
	s_waitcnt lgkmcnt(3)
	v_mfma_f32_16x16x32_f16 v[44:47], v[68:71], v[10:13], v[44:47]
	v_lshlrev_b32_e32 v60, 8, v52
	v_lshlrev_b32_e32 v52, 2, v52
	v_and_b32_e32 v52, 12, v52
	v_mfma_f32_16x16x32_f16 v[44:47], v[56:59], v[6:9], v[44:47]
	v_or_b32_e32 v62, v52, v61
	v_bitop3_b32 v52, v236, v52, v61 bitop3:0x1e
	v_lshl_or_b32 v63, v52, 4, v60
	s_waitcnt lgkmcnt(2)
	v_mfma_f32_16x16x32_f16 v[44:47], v[72:75], v[2:5], v[44:47]
	ds_read_b128 v[52:55], v63
	v_bitop3_b32 v56, v236, v62, 4 bitop3:0x36
	v_lshl_or_b32 v84, v56, 4, v60
	s_waitcnt lgkmcnt(2)
	v_mfma_f32_16x16x32_f16 v[44:47], v[76:79], v[40:43], v[44:47]
	ds_read_b128 v[56:59], v84
	v_bitop3_b32 v68, v236, v62, 8 bitop3:0x36
	v_lshl_or_b32 v85, v68, 4, v60
	s_waitcnt lgkmcnt(2)
	v_mfma_f32_16x16x32_f16 v[110:113], v[80:83], v[106:109], v[44:47]
	ds_read_b128 v[68:71], v63 offset:49152
	v_bitop3_b32 v62, v236, v62, 12 bitop3:0x36
	v_lshl_or_b32 v60, v62, 4, v60
	ds_read_b128 v[44:47], v85
	s_waitcnt lgkmcnt(3)
	v_mfma_f32_16x16x32_f16 v[52:55], v[52:55], v[22:25], 0
	ds_read_b128 v[72:75], v60
	ds_read_b128 v[76:79], v84 offset:49152
	v_mad_u32_u24 v105, v103, 3, 2
	v_lshlrev_b32_e32 v133, 4, v105
	s_waitcnt lgkmcnt(4)
	v_mfma_f32_16x16x32_f16 v[52:55], v[56:59], v[18:21], v[52:55]
	ds_read_b128 v[56:59], v85 offset:49152
	v_add_co_u32_e32 v114, vcc, s15, v88
	s_waitcnt lgkmcnt(3)
	v_mfma_f32_16x16x32_f16 v[44:47], v[44:47], v[14:17], v[52:55]
	v_addc_co_u32_e32 v115, vcc, 0, v89, vcc
	s_waitcnt lgkmcnt(2)
	v_mfma_f32_16x16x32_f16 v[44:47], v[72:75], v[10:13], v[44:47]
	ds_read_b128 v[52:55], v60 offset:49152
	v_add_u32_e32 v60, v133, v147
	v_lshlrev_b32_e32 v72, 8, v60
	v_lshlrev_b32_e32 v60, 2, v60
	v_mfma_f32_16x16x32_f16 v[44:47], v[68:71], v[6:9], v[44:47]
	v_and_b32_e32 v60, 12, v60
	v_or_b32_e32 v68, v60, v61
	v_bitop3_b32 v60, v236, v60, v61 bitop3:0x1e
	v_lshl_or_b32 v69, v60, 4, v72
	s_waitcnt lgkmcnt(2)
	v_mfma_f32_16x16x32_f16 v[44:47], v[76:79], v[2:5], v[44:47]
	ds_read_b128 v[60:63], v69
	v_bitop3_b32 v70, v236, v68, 4 bitop3:0x36
	v_lshl_or_b32 v70, v70, 4, v72
	s_waitcnt lgkmcnt(2)
	v_mfma_f32_16x16x32_f16 v[44:47], v[56:59], v[40:43], v[44:47]
	ds_read_b128 v[56:59], v70
	v_bitop3_b32 v71, v236, v68, 8 bitop3:0x36
	v_lshl_or_b32 v71, v71, 4, v72
	s_waitcnt lgkmcnt(1)
	v_mfma_f32_16x16x32_f16 v[22:25], v[60:63], v[22:25], 0
	v_bitop3_b32 v60, v236, v68, 12 bitop3:0x36
	v_lshl_or_b32 v68, v60, 4, v72
	ds_read_b32 v210, v209
	v_mfma_f32_16x16x32_f16 v[126:129], v[52:55], v[106:109], v[44:47]
	s_nop 2
	ds_read_b128 v[44:47], v71
	ds_read_b128 v[52:55], v69 offset:49152
	ds_read_b128 v[60:63], v70 offset:49152
	s_waitcnt lgkmcnt(4)
	v_mfma_f32_16x16x32_f16 v[18:21], v[56:59], v[18:21], v[22:25]
	ds_read_b128 v[56:59], v71 offset:49152
	s_nop 1
	ds_read_b128 v[22:25], v68
	s_waitcnt lgkmcnt(4)
	v_mfma_f32_16x16x32_f16 v[14:17], v[44:47], v[14:17], v[18:21]
	v_add_co_u32_e32 v44, vcc, s5, v88
	s_movk_i32 s5, 0x3000
	s_nop 0
	ds_read_b128 v[18:21], v68 offset:49152
	s_waitcnt lgkmcnt(1)
	v_mfma_f32_16x16x32_f16 v[10:13], v[22:25], v[10:13], v[14:17]
	v_addc_co_u32_e32 v45, vcc, 0, v89, vcc
	v_mfma_f32_16x16x32_f16 v[6:9], v[52:55], v[6:9], v[10:13]
	v_mov_b32_e32 v13, 0xff61b1e6
	v_mfma_f32_16x16x32_f16 v[2:5], v[60:63], v[2:5], v[6:9]
	s_nop 2
	v_add_co_u32_e32 v6, vcc, s5, v88
	v_mfma_f32_16x16x32_f16 v[2:5], v[56:59], v[40:43], v[2:5]
	s_nop 0
	v_addc_co_u32_e32 v7, vcc, 0, v89, vcc
	s_waitcnt lgkmcnt(0)
	v_mfma_f32_16x16x32_f16 v[16:19], v[18:21], v[106:109], v[2:5]
	s_mov_b32 s5, 0xff61b1e6
	s_nop 0
	v_or_b32_e32 v3, s14, v146
	v_mov_b32_e32 v4, 0x7df
	v_med3_u32 v3, v3, 32, v4
	v_or_b32_e32 v4, v97, v102
	v_sub_u32_e32 v3, v4, v3
	v_add_f32_e32 v2, s4, v210
	v_add_u32_e32 v3, 32, v3
	v_mad_u32_u24 v4, v103, 48, v3
	s_movk_i32 s4, 0x41
	v_add_f32_e32 v5, v2, v110
	v_mul_f32_e32 v5, 0x3db8aa3b, v5
	v_cmp_gt_u32_e32 vcc, s4, v4
	v_add_u32_e32 v6, 1, v4
	v_add_f32_e32 v7, v2, v111
	v_cndmask_b32_e32 v5, v13, v5, vcc
	v_mul_f32_e32 v7, 0x3db8aa3b, v7
	v_cmp_gt_u32_e32 vcc, s4, v6
	v_add_u32_e32 v8, 2, v4
	v_add_f32_e32 v9, v2, v112
	v_cndmask_b32_e32 v6, v13, v7, vcc
	v_mul_f32_e32 v9, 0x3db8aa3b, v9
	v_cmp_gt_u32_e32 vcc, s4, v8
	v_add_u32_e32 v4, 3, v4
	v_max3_f32 v7, v5, s5, v6
	v_cndmask_b32_e32 v8, v13, v9, vcc
	v_add_f32_e32 v9, v2, v113
	v_mul_f32_e32 v9, 0x3db8aa3b, v9
	v_cmp_gt_u32_e32 vcc, s4, v4
	v_add_u32_e32 v11, v3, v132
	v_add_f32_e32 v12, v2, v127
	v_cndmask_b32_e32 v10, v13, v9, vcc
	v_max3_f32 v4, v7, v8, v10
	v_add_f32_e32 v7, v2, v126
	v_mul_f32_e32 v7, 0x3db8aa3b, v7
	v_cmp_gt_u32_e32 vcc, s4, v11
	v_add_u32_e32 v9, 1, v11
	v_mul_f32_e32 v12, 0x3db8aa3b, v12
	v_cndmask_b32_e32 v7, v13, v7, vcc
	v_cmp_gt_u32_e32 vcc, s4, v9
	v_add_f32_e32 v14, v2, v128
	v_mul_f32_e32 v14, 0x3db8aa3b, v14
	v_cndmask_b32_e32 v9, v13, v12, vcc
	v_add_u32_e32 v12, 2, v11
	v_cmp_gt_u32_e32 vcc, s4, v12
	v_add_u32_e32 v11, 3, v11
	v_add_u32_e32 v3, v3, v133
	v_cndmask_b32_e32 v12, v13, v14, vcc
	v_add_f32_e32 v14, v2, v129
	v_mul_f32_e32 v14, 0x3db8aa3b, v14
	v_cmp_gt_u32_e32 vcc, s4, v11
	v_add_f32_e32 v11, v2, v16
	v_mul_f32_e32 v11, 0x3db8aa3b, v11
	v_cndmask_b32_e32 v15, v13, v14, vcc
	v_cmp_gt_u32_e32 vcc, s4, v3
	v_add_u32_e32 v14, 1, v3
	v_add_f32_e32 v16, v2, v17
	v_cndmask_b32_e32 v11, v13, v11, vcc
	v_mul_f32_e32 v16, 0x3db8aa3b, v16
	v_cmp_gt_u32_e32 vcc, s4, v14
	v_add_f32_e32 v17, v2, v18
	v_max3_f32 v4, v4, v7, v9
	v_cndmask_b32_e32 v14, v13, v16, vcc
	v_add_u32_e32 v16, 2, v3
	v_mul_f32_e32 v17, 0x3db8aa3b, v17
	v_cmp_gt_u32_e32 vcc, s4, v16
	v_add_u32_e32 v3, 3, v3
	v_add_f32_e32 v2, v2, v19
	v_max3_f32 v4, v4, v12, v15
	v_cndmask_b32_e32 v16, v13, v17, vcc
	v_mul_f32_e32 v2, 0x3db8aa3b, v2
	v_cmp_gt_u32_e32 vcc, s4, v3
	v_max3_f32 v4, v4, v11, v14
	v_lshlrev_b32_e32 v126, 5, v99
	v_cndmask_b32_e32 v17, v13, v2, vcc
	v_max3_f32 v2, v4, v16, v17
	v_mov_b32_e32 v3, v2
	v_lshlrev_b32_e32 v127, 2, v119
	v_lshrrev_b32_e32 v4, 7, v0
	v_cmp_gt_u32_e32 vcc, 16, v98
	v_permlane16_swap_b32_e32 v3, v2
	v_max_f32_e32 v2, v2, v3
	v_mov_b32_e32 v3, v2
	s_nop 1
	v_permlane32_swap_b32_e32 v3, v2
	v_max_f32_e32 v13, v2, v3
	v_and_b32_e32 v2, 0x180, v0
	v_or_b32_e32 v2, 0x23400, v2
	v_lshlrev_b32_e32 v3, 2, v100
	s_and_saveexec_b64 s[4:5], vcc
	v_lshlrev_b32_e32 v18, 6, v103
	v_add3_u32 v18, v2, v18, v3
	ds_write_b32 v18, v13
	s_or_b64 exec, exec, s[4:5]
	v_lshlrev_b32_e32 v18, 4, v103
	v_bitop3_b32 v19, v18, 16, v100 bitop3:0x36
	v_lshl_add_u32 v2, v19, 2, v2
	s_waitcnt lgkmcnt(0)
	s_barrier
	v_lshlrev_b32_e32 v232, 14, v99
	v_lshl_or_b32 v232, v98, 4, v232
	v_add_u32_e32 v233, 0x1000, v232
	v_add_u32_e32 v234, 0x2000, v232
	v_add_u32_e32 v235, 0x3000, v232
	ds_read_b32 v19, v2
	v_max_f32_e32 v13, v13, v13
	v_mul_u32_u24_e32 v20, 0xd00, v4
	s_load_dwordx2 s[0:1], s[0:1], 0x30
	v_or_b32_e32 v2, 1, v124
	s_waitcnt lgkmcnt(0)
	v_max_f32_e32 v19, v19, v19
	v_max_f32_e32 v19, v13, v19
	v_sub_f32_e32 v5, v5, v19
	v_exp_f32_e32 v5, v5
	global_load_dwordx4 v[36:39], v232, s[20:21]
	v_sub_f32_e32 v6, v6, v19
	v_exp_f32_e32 v6, v6
	v_sub_f32_e32 v8, v8, v19
	v_mul_u32_u24_e32 v13, 0xd0, v100
	v_exp_f32_e32 v8, v8
	v_sub_f32_e32 v10, v10, v19
	v_add3_u32 v20, v13, v20, v29
	v_exp_f32_e32 v10, v10
	v_or_b32_e32 v22, 0x20000, v20
	v_add_f32_e32 v20, 0, v5
	global_load_dwordx4 v[32:35], v232, s[20:21] offset:1024
	v_add_f32_e32 v20, v20, v6
	v_add_f32_e32 v20, v20, v8
	v_add_f32_e32 v23, v20, v10
	v_cvt_pk_f16_f32 v21, v8, v10
	v_cvt_pk_f16_f32 v20, v5, v6
	v_mad_u32_u24 v5, v103, s16, v22
	ds_write_b64 v5, v[20:21]
	v_sub_f32_e32 v5, v7, v19
	v_exp_f32_e32 v5, v5
	v_sub_f32_e32 v6, v9, v19
	global_load_dwordx4 v[64:67], v232, s[20:21] offset:2048
	v_exp_f32_e32 v6, v6
	v_sub_f32_e32 v7, v12, v19
	v_exp_f32_e32 v7, v7
	v_sub_f32_e32 v8, v15, v19
	v_exp_f32_e32 v8, v8
	v_sub_f32_e32 v10, v11, v19
	v_add_f32_e32 v9, v23, v5
	v_exp_f32_e32 v10, v10
	v_sub_f32_e32 v11, v14, v19
	v_add_f32_e32 v9, v9, v6
	global_load_dwordx4 v[48:51], v232, s[20:21] offset:3072
	v_exp_f32_e32 v11, v11
	v_sub_f32_e32 v12, v16, v19
	v_add_f32_e32 v9, v9, v7
	v_exp_f32_e32 v12, v12
	v_sub_f32_e32 v14, v17, v19
	v_add_f32_e32 v9, v9, v8
	v_exp_f32_e32 v14, v14
	v_add_f32_e32 v9, v9, v10
	v_add_f32_e32 v9, v9, v11
	v_add_f32_e32 v9, v9, v12
	v_add_f32_e32 v9, v9, v14
	v_mov_b32_e32 v15, v9
	v_cvt_pk_f16_f32 v7, v7, v8
	v_cvt_pk_f16_f32 v6, v5, v6
	v_lshl_add_u32 v5, v104, 5, v22
	ds_write_b64 v5, v[6:7]
	v_permlane16_swap_b32_e32 v15, v9
	v_add_f32_e32 v5, v9, v15
	v_mov_b32_e32 v6, v5
	s_movk_i32 s7, 0xd00
	s_mov_b32 s6, 0x20000
	v_cvt_pk_f16_f32 v9, v12, v14
	v_cvt_pk_f16_f32 v8, v10, v11
	v_lshl_add_u32 v7, v105, 5, v22
	ds_write_b64 v7, v[8:9]
	v_permlane32_swap_b32_e32 v6, v5
	s_and_saveexec_b64 s[4:5], vcc
	s_cbranch_execz .LBB1_4
	v_lshlrev_b32_e32 v4, 5, v4
	v_or_b32_e32 v7, v18, v100
	v_lshlrev_b32_e32 v4, 2, v4
	v_lshlrev_b32_e32 v7, 2, v7
	s_mov_b32 s8, 0x23600
	v_add3_u32 v4, v7, v4, s8
	v_add_f32_e32 v5, v5, v6
	ds_write_b32 v4, v5
